# attn: key-tile rotation (2qb+17head)&31
# baseline (speedup 1.0000x reference)
.Lp_top:
	s_lshl_b32 s6, s21, 20
	s_add_u32 s4, s4, s6
	s_addc_u32 s5, s5, 0
	v_lshlrev_b32_e32 v54, 4, v0
	v_mov_b32_e32 v55, v63
	s_lshl_b32 s3, s3, 1
	s_mul_i32 s20, s21, 17
	v_lshl_add_u64 v[4:5], s[4:5], 0, v[54:55]
	s_mov_b64 s[4:5], 0x1000000
	s_add_i32 s20, s20, s3
	v_lshl_add_u64 v[170:171], v[4:5], 0, s[4:5]
	s_and_b32 s22, s20, 31
	s_lshl_b32 s4, s20, 12
	s_lshl_b32 s12, s22, 13
	s_add_i32 s5, s4, 0x1000
	v_lshl_add_u64 v[58:59], v[170:171], 0, s[12:13]
	s_mov_b32 s3, 0x80000
	s_and_b32 s5, s5, 0x1f000
	v_add_co_u32_e32 v16, vcc, s3, v58
	s_lshl_b32 s12, s5, 1
	s_nop 0
	v_addc_co_u32_e32 v17, vcc, 0, v59, vcc
	v_lshl_add_u64 v[56:57], v[170:171], 0, s[12:13]
	global_load_dwordx4 v[4:7], v[58:59], off
	global_load_dwordx4 v[8:11], v[56:57], off
	global_load_dwordx4 v[12:15], v[16:17], off
	v_add_co_u32_e32 v16, vcc, s3, v56
	v_lshrrev_b32_e32 v184, 8, v0
	s_nop 0
	v_addc_co_u32_e32 v17, vcc, 0, v57, vcc
	global_load_dwordx4 v[16:19], v[16:17], off
	v_and_b32_e32 v20, 19, v0
	v_lshlrev_b32_e32 v21, 1, v0
	v_and_b32_e32 v2, 4, v2
	v_and_or_b32 v20, v21, 8, v20
	v_lshlrev_b32_e32 v101, 5, v184
	s_addk_i32 s4, 0x2000
	v_or3_b32 v2, v20, v2, v101
	s_and_b32 s4, s4, 0x1f000
	v_mul_u32_u24_e32 v2, 0x48, v2
	s_lshl_b32 s12, s4, 1
	v_lshlrev_b32_e32 v3, 3, v0
	v_lshlrev_b32_e32 v100, 1, v99
	v_lshlrev_b32_e32 v2, 1, v2
	v_lshl_add_u64 v[60:61], v[170:171], 0, s[12:13]
	v_and_b32_e32 v3, 56, v3
	v_add3_u32 v186, 0, v2, v100
	v_add_co_u32_e32 v2, vcc, s3, v60
	v_lshlrev_b32_e32 v68, 1, v3
	s_nop 0
	v_addc_co_u32_e32 v3, vcc, 0, v61, vcc
	global_load_dwordx4 v[162:165], v[60:61], off
	global_load_dwordx4 v[166:169], v[2:3], off
	v_lshrrev_b32_e32 v82, 3, v0
	v_mul_u32_u24_e32 v22, 0x48, v82
	v_lshlrev_b32_e32 v21, 1, v22
	v_add3_u32 v185, 0, v21, v68
	s_mov_b64 s[24:25], 0x80000
	s_add_i32 s17, s20, 3
	s_add_i32 s18, s20, 4
	v_mov_b32_e32 v62, v63
	v_lshrrev_b32_e32 v55, 6, v0
	v_mov_b32_e32 v83, 0
	v_mov_b32_e32 v84, 0
	v_lshl_add_u64 v[70:71], v[58:59], 0, s[24:25]
	v_lshl_add_u64 v[66:67], v[56:57], 0, s[24:25]
	v_lshl_add_u64 v[64:65], v[60:61], 0, s[24:25]
	s_waitcnt vmcnt(5)
	ds_write_b128 v185, v[4:7]
	s_waitcnt vmcnt(3)
	ds_write_b128 v185, v[12:15] offset:9216
	ds_write_b128 v185, v[8:11] offset:18432
	s_waitcnt vmcnt(2)
	ds_write_b128 v185, v[16:19] offset:27648
	s_waitcnt lgkmcnt(0)
	s_barrier
	ds_read_b128 v[2:5], v186
	ds_read_b128 v[38:41], v186 offset:32
	s_waitcnt lgkmcnt(1)
	v_mfma_f32_32x32x16_f16 v[2:17], v[2:5], v[114:117], 0
	ds_read_b128 v[18:21], v186 offset:9216
	ds_read_b128 v[46:49], v186 offset:9248
	s_waitcnt lgkmcnt(1)
	v_mfma_f32_32x32x16_f16 v[18:33], v[18:21], v[130:133], 0
	v_mfma_f32_32x32x16_f16 v[2:17], v[38:41], v[118:121], v[2:17]
	s_waitcnt lgkmcnt(0)
	v_mfma_f32_32x32x16_f16 v[18:33], v[46:49], v[134:137], v[18:33]
	ds_read_b128 v[38:41], v186 offset:64
	ds_read_b128 v[46:49], v186 offset:96
	s_waitcnt lgkmcnt(1)
	v_mfma_f32_32x32x16_f16 v[2:17], v[38:41], v[122:125], v[2:17]
	ds_read_b128 v[38:41], v186 offset:9280
	ds_read_b128 v[50:53], v186 offset:9312
	s_load_dwordx4 s[4:7], s[0:1], 0x38
	s_load_dwordx2 s[14:15], s[0:1], 0x8
	s_mov_b32 s0, -2
	s_mov_b32 s1, 0x3f800000
	s_waitcnt lgkmcnt(0)
	s_barrier
	v_mfma_f32_32x32x16_f16 v[18:33], v[38:41], v[138:141], v[18:33]
	v_mfma_f32_32x32x16_f16 v[2:17], v[46:49], v[126:129], v[2:17]
	v_mfma_f32_32x32x16_f16 v[18:33], v[50:53], v[142:145], v[18:33]
	s_lshl_b32 s12, s17, 13
	s_and_b32 s12, s12, 0x3e000
	s_add_u32 s28, s12, s3
	s_mov_b32 s29, 0
	v_lshl_add_u64 v[176:177], v[170:171], 0, s[12:13]
	global_load_dwordx4 v[50:53], v[176:177], off
	v_lshl_add_u64 v[176:177], v[170:171], 0, s[28:29]
	global_load_dwordx4 v[94:97], v[176:177], off
	s_nop 7
	s_cmp_eq_u32 s37, 1
	s_cbranch_scc0 .Lf_A
	v_mov_b32_e32 v83, 0xf149f2ca
	v_mov_b32_e32 v84, 0xf149f2ca
	s_branch .Ls_A

.Ll1_cont:
	ds_bpermute_b32 v2, v69, v84
	ds_bpermute_b32 v5, v69, v83
	v_max_f32_e32 v4, v84, v84
	v_max_f32_e32 v7, v83, v83
	ds_bpermute_b32 v3, v69, v63
	s_waitcnt lgkmcnt(2)
	v_max_f32_e32 v6, v2, v2
	v_max_f32_e32 v4, v4, v6
	v_sub_f32_e32 v6, v84, v4
	v_exp_f32_e32 v9, v6
	s_waitcnt lgkmcnt(1)
	v_max_f32_e32 v6, v5, v5
	v_sub_f32_e32 v2, v2, v4
	v_max_f32_e32 v6, v7, v6
	v_exp_f32_e32 v11, v2
	ds_bpermute_b32 v2, v69, v62
	v_sub_f32_e32 v5, v5, v6
	v_sub_f32_e32 v7, v83, v6
	v_exp_f32_e32 v10, v5
	v_exp_f32_e32 v8, v7
	v_cmp_gt_u32_e32 vcc, 32, v98
	s_waitcnt lgkmcnt(0)
	v_pk_mul_f32 v[2:3], v[10:11], v[2:3]
	s_nop 0
	v_pk_fma_f32 v[8:9], v[62:63], v[8:9], v[2:3]
	v_lshlrev_b32_e32 v2, 7, v184
	v_or3_b32 v10, v183, v2, v1
	s_and_saveexec_b64 s[0:1], vcc
	v_lshl_add_u32 v2, v10, 4, 0
	v_add_u32_e32 v2, 0x21000, v2
	v_mov_b32_e32 v5, v9
	v_mov_b32_e32 v7, v8
	ds_write_b128 v2, v[4:7]
	s_or_b64 exec, exec, s[0:1]
	s_lshl_b32 s12, s21, 7
	s_mov_b32 s3, 0
	v_or_b32_e32 v2, s12, v82
	s_lshl_b32 s13, s21, 11
	s_add_i32 s23, 0, 0x12000
	v_lshlrev_b32_e32 v2, 12, v2
	v_mov_b32_e32 v3, 0
	s_add_i32 s13, s13, s16
	s_lshl_b64 s[0:1], s[2:3], 13
	v_lshl_add_u64 v[12:13], s[14:15], 0, v[2:3]
	v_mov_b32_e32 v69, v3
	s_add_u32 s0, s10, s0
	v_lshl_add_u64 v[172:173], v[12:13], 0, v[68:69]
	s_addc_u32 s1, s11, s1
	s_lshl_b32 s10, s22, 7
	s_mov_b32 s11, s3
	s_waitcnt vmcnt(1)
	v_lshl_add_u64 v[36:37], v[172:173], 0, s[10:11]
	s_mov_b32 s10, 0x40000
	v_add_co_u32_e32 v38, vcc, s10, v36
	s_waitcnt lgkmcnt(0)
	s_barrier
	global_load_dwordx4 v[12:15], v[58:59], off
	global_load_dwordx4 v[16:19], v[70:71], off
	v_addc_co_u32_e32 v39, vcc, 0, v37, vcc
	global_load_dwordx4 v[20:23], v[56:57], off
	global_load_dwordx4 v[24:27], v[66:67], off
	global_load_dwordx4 v[28:31], v[36:37], off
	global_load_dwordx4 v[32:35], v[38:39], off
	v_add_f32_e32 v2, v78, v80
	s_movk_i32 s11, 0x1200
	v_add_f32_e32 v5, v79, v81
	s_mov_b32 s14, 0x3fb8aa3b
	v_lshlrev_b32_e32 v10, 4, v10
	v_mov_b32_e32 v36, s23
	v_mul_f32_e32 v37, 0x3fb8aa3b, v2
	v_mul_f32_e32 v38, 0x3fb8aa3b, v5
	v_xor_b32_e32 v10, 0x800, v10
	v_mad_u32_u24 v40, v55, s11, v36
	v_fma_f32 v36, v2, s14, -v37
	v_rndne_f32_e32 v39, v37
	v_fma_f32 v41, v5, s14, -v38
	s_waitcnt vmcnt(6)
	v_rndne_f32_e32 v42, v38
	v_add_u32_e32 v10, 0, v10
	v_fmac_f32_e32 v36, 0x32a5705f, v2
	v_sub_f32_e32 v37, v37, v39
	v_fmac_f32_e32 v41, 0x32a5705f, v5
	v_sub_f32_e32 v38, v38, v42
	v_add_u32_e32 v10, 0x21000, v10
	v_add_f32_e32 v44, v37, v36
	global_load_dwordx4 v[146:149], v[60:61], off
	global_load_dwordx4 v[150:153], v[64:65], off
	v_cvt_i32_f32_e32 v43, v39
	v_add_f32_e32 v41, v38, v41
	ds_read_b128 v[36:39], v10
	v_exp_f32_e32 v10, v44
	v_cvt_i32_f32_e32 v42, v42
	v_exp_f32_e32 v41, v41
	s_mov_b32 s21, 0xc2ce8ed0
	s_lshl_b32 s11, s20, 6
	s_add_i32 s14, s11, 64
	v_ldexp_f32 v10, v10, v43
	v_cmp_ngt_f32_e32 vcc, s21, v2
	s_mov_b32 s22, 0x42b17218
	s_and_b32 s14, s14, 0x7c0
	v_ldexp_f32 v41, v41, v42
	v_cndmask_b32_e32 v10, 0, v10, vcc
	v_cmp_ngt_f32_e32 vcc, s21, v5
	v_mov_b32_e32 v7, 0x7f800000
	v_max_f32_e32 v11, v4, v4
	s_mov_b32 s15, s3
	s_lshl_b32 s14, s14, 1
	s_waitcnt lgkmcnt(0)
	v_max_f32_e32 v42, v36, v36
	v_cndmask_b32_e32 v41, 0, v41, vcc
	v_cmp_nlt_f32_e32 vcc, s22, v2
	v_max_f32_e32 v187, v11, v42
	v_mov_b32_e32 v55, v3
	v_cndmask_b32_e32 v2, v7, v10, vcc
	v_cmp_nlt_f32_e32 vcc, s22, v5
	v_lshl_add_u64 v[10:11], v[172:173], 0, s[14:15]
	v_lshl_add_u64 v[178:179], s[0:1], 0, v[54:55]
	v_cndmask_b32_e32 v5, v7, v41, vcc
	v_sub_f32_e32 v2, v2, v5
	v_add_f32_e32 v41, 0x3e4ccccd, v2
	v_sub_f32_e32 v2, v4, v187
	v_max_f32_e32 v4, v6, v6
	s_and_b32 s1, s2, 7
	s_mulk_i32 s1, 0x880
	s_mulk_i32 s19, 0x440
	s_add_i32 s0, s20, 2
	s_waitcnt vmcnt(7)
	ds_write_b128 v185, v[12:15]
	s_waitcnt vmcnt(6)
	ds_write_b128 v185, v[16:19] offset:9216
	s_waitcnt vmcnt(5)
	ds_write_b128 v185, v[20:23] offset:18432
	s_waitcnt vmcnt(4)
	ds_write_b128 v185, v[24:27] offset:27648
	s_waitcnt vmcnt(3)
	ds_write_b128 v185, v[28:31] offset:36864
	s_waitcnt vmcnt(2)
	ds_write_b128 v185, v[32:35] offset:46080
	v_add_co_u32_e32 v12, vcc, s10, v10
	v_exp_f32_e32 v23, v2
	s_nop 0
	v_addc_co_u32_e32 v13, vcc, 0, v11, vcc
	global_load_dwordx4 v[154:157], v[10:11], off
	global_load_dwordx4 v[158:161], v[12:13], off
	s_waitcnt lgkmcnt(0)
	s_barrier
	ds_read_b128 v[10:13], v186
	v_sub_f32_e32 v2, v36, v187
	v_exp_f32_e32 v25, v2
	v_max_f32_e32 v2, v38, v38
	v_max_f32_e32 v188, v4, v2
	v_sub_f32_e32 v2, v6, v188
	v_exp_f32_e32 v22, v2
	v_sub_f32_e32 v2, v38, v188
	v_exp_f32_e32 v24, v2
	ds_read_b128 v[14:17], v186 offset:9216
	ds_read_b128 v[18:21], v186 offset:32
	s_waitcnt lgkmcnt(2)
	v_mfma_f32_32x32x16_f16 v[66:81], v[10:13], v[114:117], 0
	v_mov_b32_e32 v36, v39
	v_mul_f32_e64 v10, v36, v24
	v_mul_f32_e64 v11, v37, v25
	ds_read_b128 v[4:7], v186 offset:9248
	s_add_i32 s1, s1, s19
	s_mov_b32 s14, 0x30000
	s_mov_b32 s15, 0x80000
	s_mov_b32 s19, 0
	s_waitcnt lgkmcnt(2)
	v_mfma_f32_32x32x16_f16 v[82:97], v[14:17], v[130:133], 0
	v_fma_f32 v16, v8, v22, v10
	v_fma_f32 v17, v9, v23, v11
	v_log_f32_e32 v238, v17
	s_nop 0
	v_add_f32_e32 v187, v187, v238
	v_sub_f32_e32 v240, 0, v187
	v_sub_f32_e32 v241, 0, v187
	v_sub_f32_e32 v242, 0, v187
	v_sub_f32_e32 v243, 0, v187
	v_sub_f32_e32 v244, 0, v187
	v_sub_f32_e32 v245, 0, v187
	v_sub_f32_e32 v246, 0, v187
	v_sub_f32_e32 v247, 0, v187
	v_sub_f32_e32 v248, 0, v187
	v_sub_f32_e32 v249, 0, v187
	v_sub_f32_e32 v250, 0, v187
	v_sub_f32_e32 v251, 0, v187
	v_sub_f32_e32 v252, 0, v187
	v_sub_f32_e32 v253, 0, v187
	v_sub_f32_e32 v254, 0, v187
	v_sub_f32_e32 v255, 0, v187
	v_lshrrev_b32_e32 v22, 3, v98
	v_or3_b32 v2, s13, v183, v22
	v_lshlrev_b64 v[8:9], 13, v[2:3]
	v_lshl_add_u64 v[8:9], s[4:5], 0, v[8:9]
	v_lshlrev_b32_e32 v2, 2, v101
	v_lshl_add_u64 v[8:9], v[8:9], 0, v[2:3]
	v_and_b32_e32 v2, 0x70, v54
	v_lshl_add_u64 v[174:175], v[8:9], 0, v[2:3]
	ds_read_b128 v[8:11], v186 offset:64
	s_waitcnt lgkmcnt(2)
	v_mfma_f32_32x32x16_f16 v[66:81], v[18:21], v[118:121], v[66:81]
	v_div_scale_f32 v18, s[4:5], v16, v16, -v41
	v_rcp_f32_e32 v19, v18
	v_div_scale_f32 v20, vcc, -v41, v16, -v41
	s_mov_b32 s13, 0x20000
	v_mov_b32_e32 v24, v3
	s_waitcnt lgkmcnt(1)
	v_mfma_f32_32x32x16_f16 v[82:97], v[4:7], v[134:137], v[82:97]
	v_fma_f32 v4, -v18, v19, 1.0
	v_fmac_f32_e32 v19, v4, v19
	v_mul_f32_e32 v21, v20, v19
	ds_read_b128 v[4:7], v186 offset:9280
	ds_read_b128 v[12:15], v186 offset:96
	v_mov_b32_e32 v25, v3
	v_mov_b32_e32 v26, v3
	v_mov_b32_e32 v27, v3
	s_waitcnt lgkmcnt(2)
	v_mfma_f32_32x32x16_f16 v[66:81], v[8:11], v[122:125], v[66:81]
	v_fma_f32 v8, -v18, v21, v20
	v_fmac_f32_e32 v21, v8, v19
	v_fma_f32 v18, -v18, v21, v20
	v_div_scale_f32 v20, s[4:5], v17, v17, 1.0
	v_rcp_f32_e32 v23, v20
	ds_read_b128 v[8:11], v186 offset:9312
	s_waitcnt lgkmcnt(2)
	v_mfma_f32_32x32x16_f16 v[82:97], v[4:7], v[138:141], v[82:97]
	v_div_fmas_f32 v4, v18, v19, v21
	v_div_fixup_f32 v176, v4, v16, -v41
	v_fma_f32 v4, -v20, v23, 1.0
	v_fmac_f32_e32 v23, v4, v23
	v_div_scale_f32 v4, vcc, 1.0, v17, 1.0
	v_mul_f32_e32 v5, v4, v23
	v_fma_f32 v6, -v20, v5, v4
	v_fmac_f32_e32 v5, v6, v23
	s_waitcnt lgkmcnt(1)
	v_mfma_f32_32x32x16_f16 v[66:81], v[12:15], v[126:129], v[66:81]
	v_fma_f32 v4, -v20, v5, v4
	v_div_fmas_f32 v4, v4, v23, v5
	v_div_fixup_f32 v177, v4, v17, 1.0
	v_mul_u32_u24_e32 v4, 0x90, v22
	v_add3_u32 v189, v40, v4, v2
	v_mul_u32_u24_e32 v2, 0x90, v1
	v_lshlrev_b32_e32 v4, 2, v99
	s_waitcnt lgkmcnt(0)
	v_mfma_f32_32x32x16_f16 v[82:97], v[8:11], v[142:145], v[82:97]
	v_add3_u32 v190, v40, v2, v4
	v_mul_u32_u24_e32 v2, 0x48, v1
	v_lshl_add_u32 v2, v2, 1, 0
	v_lshlrev_b32_e32 v4, 1, v101
	v_add3_u32 v191, v2, v4, v100
	s_mov_b32 s4, 0x3f800000
	s_mov_b32 s5, 0x10000
	v_mov_b32_e32 v2, v3
	v_mov_b32_e32 v4, v3
	v_mov_b32_e32 v5, v3
	v_mov_b32_e32 v6, v3
	v_mov_b32_e32 v7, v3
	v_mov_b32_e32 v8, v3
	v_mov_b32_e32 v9, v3
	v_mov_b32_e32 v10, v3
	v_mov_b32_e32 v11, v3
	v_mov_b32_e32 v12, v3
	v_mov_b32_e32 v13, v3
	v_mov_b32_e32 v14, v3
	v_mov_b32_e32 v15, v3
	v_mov_b32_e32 v16, v3
	v_mov_b32_e32 v17, v3
	v_mov_b32_e32 v18, v3
	v_mov_b32_e32 v19, v3
	v_mov_b32_e32 v20, v3
	v_mov_b32_e32 v21, v3
	v_mov_b32_e32 v22, v3
	v_mov_b32_e32 v23, v3
	v_mov_b32_e32 v28, v3
	v_mov_b32_e32 v29, v3
	v_mov_b32_e32 v30, v3
	v_mov_b32_e32 v31, v3
	v_mov_b32_e32 v32, v3
	v_mov_b32_e32 v33, v3
	v_mov_b32_e32 v34, v3
	v_mov_b32_e32 v35, v3
	v_mov_b32_e32 v36, v3
	v_mov_b32_e32 v37, v3
	v_mov_b32_e32 v38, v3
	v_mov_b32_e32 v39, v3
	v_mov_b32_e32 v40, v3
	v_mov_b32_e32 v41, v3
	v_mov_b32_e32 v42, v3
	v_mov_b32_e32 v43, v3
	v_mov_b32_e32 v44, v3
	v_mov_b32_e32 v45, v3
	v_mov_b32_e32 v46, v3
	v_mov_b32_e32 v47, v3
	v_mov_b32_e32 v48, v3
	v_mov_b32_e32 v49, v3
	v_mov_b32_e32 v50, v3
	v_mov_b32_e32 v51, v3
	v_mov_b32_e32 v52, v3
	v_mov_b32_e32 v53, v3
	v_mov_b32_e32 v54, v3
	v_mov_b32_e32 v56, v3
	v_mov_b32_e32 v57, v3
	v_mov_b32_e32 v58, v3
	v_mov_b32_e32 v59, v3
	v_mov_b32_e32 v60, v3
	v_mov_b32_e32 v61, v3
	v_mov_b32_e32 v62, v3
	v_mov_b32_e32 v63, v3
	v_mov_b32_e32 v64, v3
	v_mov_b32_e32 v65, v3
	v_add_u32_e32 v192, 0xd800, v191
	v_sub_f32_e32 v66, v66, v187
	v_sub_f32_e32 v67, v67, v187
	v_sub_f32_e32 v68, v68, v187
	v_sub_f32_e32 v69, v69, v187
	v_sub_f32_e32 v70, v70, v187
	v_sub_f32_e32 v71, v71, v187
	v_sub_f32_e32 v72, v72, v187
	v_sub_f32_e32 v73, v73, v187
	v_sub_f32_e32 v74, v74, v187
	v_sub_f32_e32 v75, v75, v187
	v_sub_f32_e32 v76, v76, v187
	v_sub_f32_e32 v77, v77, v187
	v_sub_f32_e32 v78, v78, v187
	v_sub_f32_e32 v79, v79, v187
	v_sub_f32_e32 v80, v80, v187
	v_sub_f32_e32 v81, v81, v187
	s_mov_b32 s27, 0x42c80000
	v_cmp_gt_f32_e64 vcc, |v188|, s27
	s_cbranch_vccnz .Ll2_gen
	v_sub_f32_e32 v238, 0, v188
	v_exp_f32_e32 v238, v238
	s_nop 0
	v_mul_f32_e32 v176, v176, v238
	s_barrier
	s_branch .Ll2f_top
